# speedup vs baseline: 1.0260x; 1.0260x over previous
	.amdhsa_kernel _Z16sum_layer_kernelPKfS0_Pf
		.amdhsa_group_segment_fixed_size 18432
		.amdhsa_private_segment_fixed_size 0
		.amdhsa_kernarg_size 24
		.amdhsa_user_sgpr_count 2
		.amdhsa_user_sgpr_dispatch_ptr 0
		.amdhsa_user_sgpr_queue_ptr 0
		.amdhsa_user_sgpr_kernarg_segment_ptr 1
		.amdhsa_user_sgpr_dispatch_id 0
		.amdhsa_user_sgpr_kernarg_preload_length 0
		.amdhsa_user_sgpr_kernarg_preload_offset 0
		.amdhsa_user_sgpr_private_segment_size 0
		.amdhsa_uses_dynamic_stack 0
		.amdhsa_enable_private_segment 0
		.amdhsa_system_sgpr_workgroup_id_x 1
		.amdhsa_system_sgpr_workgroup_id_y 0
		.amdhsa_system_sgpr_workgroup_id_z 0
		.amdhsa_system_sgpr_workgroup_info 0
		.amdhsa_system_vgpr_workitem_id 0
		.amdhsa_next_free_vgpr 120
		.amdhsa_next_free_sgpr 16
		.amdhsa_accum_offset 120
		.amdhsa_reserve_vcc 1
		.amdhsa_float_round_mode_32 0
		.amdhsa_float_round_mode_16_64 0
		.amdhsa_float_denorm_mode_32 3
		.amdhsa_float_denorm_mode_16_64 3
		.amdhsa_dx10_clamp 1
		.amdhsa_ieee_mode 1
		.amdhsa_fp16_overflow 0
		.amdhsa_tg_split 0
		.amdhsa_exception_fp_ieee_invalid_op 0
		.amdhsa_exception_fp_denorm_src 0
		.amdhsa_exception_fp_ieee_div_zero 0
		.amdhsa_exception_fp_ieee_overflow 0
		.amdhsa_exception_fp_ieee_underflow 0
		.amdhsa_exception_fp_ieee_inexact 0
		.amdhsa_exception_int_div_zero 0
	.end_amdhsa_kernel

amdhsa.kernels:
  - .agpr_count:     0
    .args:
      - .address_space:  global
        .offset:         0
        .size:           8
        .value_kind:     global_buffer
      - .address_space:  global
        .offset:         8
        .size:           8
        .value_kind:     global_buffer
      - .address_space:  global
        .offset:         16
        .size:           8
        .value_kind:     global_buffer
    .group_segment_fixed_size: 18432
    .kernarg_segment_align: 8
    .kernarg_segment_size: 24
    .language:       OpenCL C
    .language_version:
      - 2
      - 0
    .max_flat_workgroup_size: 256
    .name:           _Z16sum_layer_kernelPKfS0_Pf
    .private_segment_fixed_size: 0
    .sgpr_count:     22
    .sgpr_spill_count: 0
    .symbol:         _Z16sum_layer_kernelPKfS0_Pf.kd
    .uniform_work_group_size: 1
    .uses_dynamic_stack: false
    .vgpr_count:     120
    .vgpr_spill_count: 0
    .wavefront_size: 64
